# wait pruning: P2 gate-epilogue tail throttling waits (bb.429, join) removed, on top of v83 (v82 + final-norm loop-head wait removed)
# speedup vs baseline: 1.0016x; 1.0016x over previous
.LBB0_428:
	s_andn2_b64 vcc, exec, s[0:1]
	s_cbranch_vccnz .LBB0_430
	v_mul_f32_e32 v131, 0xbfb8aa3b, v2
	v_mul_f32_e32 v132, 0xbfb8aa3b, v7
	v_exp_f32_e32 v131, v131
	v_exp_f32_e32 v133, v132
	v_mul_f32_e32 v135, 0xbfb8aa3b, v4
	v_mul_f32_e32 v136, 0xbfb8aa3b, v9
	v_add_f32_e32 v131, 1.0, v131
	v_mul_f32_e32 v130, 0xbfb8aa3b, v6
	v_rcp_f32_e32 v132, v131
	v_add_f32_e32 v131, 1.0, v133
	v_mul_f32_e32 v133, 0xbfb8aa3b, v3
	v_mul_f32_e32 v134, 0xbfb8aa3b, v8
	v_exp_f32_e32 v135, v135
	v_exp_f32_e32 v137, v136
	v_mul_f32_e32 v136, 0xbfb8aa3b, v5
	v_exp_f32_e32 v130, v130
	v_exp_f32_e32 v133, v133
	v_exp_f32_e32 v134, v134
	v_exp_f32_e32 v146, v136
	v_add_f32_e32 v135, 1.0, v135
	v_add_f32_e32 v130, 1.0, v130
	v_add_f32_e32 v133, 1.0, v133
	v_add_f32_e32 v134, 1.0, v134
	v_rcp_f32_e32 v136, v135
	v_add_f32_e32 v135, 1.0, v137
	v_add_f32_e32 v137, 1.0, v146
	v_rcp_f32_e32 v130, v130
	v_rcp_f32_e32 v131, v131
	v_rcp_f32_e32 v134, v134
	v_rcp_f32_e32 v135, v135
	v_rcp_f32_e32 v137, v137
	v_rcp_f32_e32 v133, v133
	v_pk_mul_f32 v[170:171], v[6:7], v[130:131]
	v_pk_mul_f32 v[174:175], v[8:9], v[134:135]
	v_pk_mul_f32 v[176:177], v[4:5], v[136:137]
	v_pk_mul_f32 v[172:173], v[2:3], v[132:133]
.LBB0_430:
	v_lshl_add_u64 v[134:135], v[184:185], 0, s[38:39]
	v_cvt_pk_bf16_f32 v130, v170, v171
	v_cvt_pk_bf16_f32 v131, v174, v175
	v_cvt_pk_bf16_f32 v132, v172, v173
	v_cvt_pk_bf16_f32 v133, v176, v177
	global_store_dwordx4 v[134:135], v[130:133], off offset:256
